# baseline (speedup 1.0000x reference)
_Z6k_agg1PKiS0_PK6__halfPKfS5_S5_S3_S5_S5_PS1_PfS7_S5_S0_S0_:
	s_and_b32 s3, s2, 7
	s_mul_i32 s5, s3, 0x30d
	s_min_u32 s3, s3, 2
	s_lshr_b32 s2, s2, 3
	v_readfirstlane_b32 s36, v0
	s_add_i32 s2, s3, s2
	s_lshr_b32 s4, s36, 6
	s_add_i32 s2, s2, s5
	s_load_dwordx4 s[8:11], s[0:1], 0x60
	s_lshl_b32 s33, s2, 4
	s_lshl_b32 s2, s4, 2
	v_bfe_u32 v42, v0, 4, 2
	s_add_i32 s2, s2, s33
	v_or_b32_e32 v2, s2, v42
	v_ashrrev_i32_e32 v3, 31, v2
	v_lshlrev_b64 v[10:11], 2, v[2:3]
	s_load_dwordx2 s[2:3], s[0:1], 0x70
	s_waitcnt lgkmcnt(0)
	v_lshl_add_u64 v[2:3], s[10:11], 0, v[10:11]
	global_load_dword v1, v[2:3], off
	s_load_dwordx2 s[6:7], s[0:1], 0x20
	s_load_dwordx2 s[26:27], s[0:1], 0x8
	v_and_b32_e32 v44, 15, v0
	v_lshlrev_b32_e32 v77, 4, v10
	v_lshl_add_u32 v77, v44, 2, v77
	s_sub_u32 s38, s10, 13200128
	s_subb_u32 s39, s11, 0
	v_lshlrev_b32_e32 v12, 5, v44
	v_lshl_add_u64 v[10:11], s[2:3], 0, v[10:11]
	global_load_dwordx4 v[2:5], v12, s[8:9] offset:16
	global_load_dwordx4 v[6:9], v12, s[8:9]
	global_load_dword v48, v[10:11], off
	v_mov_b32_e32 v33, 0
	v_and_b32_e32 v32, 12, v0
	v_mov_b32_e32 v52, 0
	s_waitcnt vmcnt(3)
	v_ashrrev_i32_e32 v46, 24, v1
	v_add_u32_e32 v10, s33, v46
	v_ashrrev_i32_e32 v11, 31, v10
	s_waitcnt lgkmcnt(0)
	v_lshl_add_u64 v[10:11], v[10:11], 4, s[6:7]
	v_lshl_add_u64 v[10:11], v[10:11], 0, v[32:33]
	global_load_dword v50, v[10:11], off
	v_and_b32_e32 v51, 0xffffff, v1
	v_add_u32_e32 v1, v51, v44
	s_waitcnt vmcnt(1)
	v_cmp_lt_i32_e32 vcc, v1, v48
	s_and_saveexec_b64 s[2:3], vcc
	s_cbranch_execz .LBB3_2
	v_lshlrev_b32_e32 v1, 2, v1
	global_load_dword v52, v1, s[26:27]
.LBB3_2:
	s_or_b64 exec, exec, s[2:3]
	s_load_dwordx2 s[20:21], s[0:1], 0x58
	s_load_dwordx2 s[24:25], s[0:1], 0x28
	s_load_dwordx2 s[22:23], s[0:1], 0x40
	v_lshlrev_b32_e32 v49, 3, v44
	v_and_b32_e32 v43, 63, v0
	v_lshlrev_b32_e32 v47, 4, v44
	v_and_b32_e32 v45, 48, v0
	v_cmp_gt_i32_e32 vcc, v48, v51
	v_mov_b32_e32 v32, 0
	v_mov_b32_e32 v35, 0
	v_mov_b32_e32 v34, 0
	v_mov_b32_e32 v37, 0
	v_mov_b32_e32 v36, 0
	v_mov_b32_e32 v39, 0
	v_mov_b32_e32 v38, 0
	v_mov_b32_e32 v64, 0
	s_and_saveexec_b64 s[28:29], vcc
	s_cbranch_execz .LBB3_12
	s_load_dwordx2 s[16:17], s[0:1], 0x10
	s_lshl_b32 s2, s4, 8
	s_addk_i32 s2, 0x1100
	v_cvt_pk_f16_f32 v53, v6, v7
	v_cvt_pk_f16_f32 v54, v8, v9
	v_cvt_pk_f16_f32 v55, v2, v3
	v_cvt_pk_f16_f32 v56, v4, v5
	s_mov_b32 s19, 0x20000
	s_mov_b32 s18, 0x186a000
	s_waitcnt lgkmcnt(0)
	s_and_b32 s17, s17, 0xffff
	v_lshl_or_b32 v57, v43, 2, s2
	v_lshl_or_b32 v58, v45, 2, s2
	v_sub_u32_e32 v59, v48, v51
	v_add_u32_e32 v60, -9, v48
	v_add_u32_e32 v61, -1, v48
	v_mov_b32_e32 v41, 0
	v_mov_b32_e32 v62, 0xff800000
	s_mov_b64 s[30:31], 0
	v_bfrev_b32_e32 v63, 1
	v_mov_b32_e32 v65, 0xff800000
	v_mov_b32_e32 v64, 0
	v_mov_b32_e32 v38, 0
	v_mov_b32_e32 v39, 0
	v_mov_b32_e32 v36, 0
	v_mov_b32_e32 v37, 0
	v_mov_b32_e32 v34, 0
	v_mov_b32_e32 v35, 0
	v_mov_b32_e32 v32, 0
	v_mov_b32_e32 v33, 0
	s_waitcnt vmcnt(0)
	v_mov_b32_e32 v78, v52
	s_branch .LBB3_5

.LBB3_12:
	s_or_b64 exec, exec, s[28:29]
	v_lshlrev_b32_e32 v8, 2, v49
	s_load_dwordx2 s[2:3], s[0:1], 0x48
	s_load_dwordx2 s[6:7], s[0:1], 0x30
	s_waitcnt lgkmcnt(0)
	global_load_dwordx4 v[0:3], v8, s[24:25]
	global_load_dwordx4 v[4:7], v8, s[24:25] offset:16
	v_rcp_f32_e32 v8, v64
	s_cmp_lt_u32 s36, 64
	s_movk_i32 s0, 0x110
	s_cselect_b64 s[4:5], -1, 0
	v_cndmask_b32_e32 v8, 0, v8, vcc
	v_mad_i32_i24 v16, v46, s0, v47
	s_and_b64 s[0:1], exec, s[4:5]
	s_waitcnt vmcnt(1)
	v_pk_fma_f32 v[0:1], v[38:39], v[8:9], v[0:1] op_sel_hi:[1,0,1]
	v_pk_fma_f32 v[2:3], v[36:37], v[8:9], v[2:3] op_sel_hi:[1,0,1]
	s_waitcnt vmcnt(0)
	v_pk_fma_f32 v[4:5], v[34:35], v[8:9], v[4:5] op_sel_hi:[1,0,1]
	v_pk_fma_f32 v[6:7], v[32:33], v[8:9], v[6:7] op_sel_hi:[1,0,1]
	v_mul_f32_e32 v8, 0x3fb8aa3b, v0
	v_mul_f32_e32 v9, 0x3fb8aa3b, v1
	v_exp_f32_e32 v8, v8
	v_exp_f32_e32 v9, v9
	v_mul_f32_e32 v10, 0x3fb8aa3b, v2
	v_mul_f32_e32 v11, 0x3fb8aa3b, v3
	v_exp_f32_e32 v10, v10
	v_exp_f32_e32 v11, v11
	v_mul_f32_e32 v12, 0x3fb8aa3b, v4
	v_mul_f32_e32 v13, 0x3fb8aa3b, v5
	v_exp_f32_e32 v12, v12
	v_exp_f32_e32 v13, v13
	v_pk_add_f32 v[8:9], v[8:9], -1.0 op_sel_hi:[1,0]
	v_cmp_lt_f32_e32 vcc, 0, v1
	v_mul_f32_e32 v14, 0x3fb8aa3b, v6
	v_mul_f32_e32 v15, 0x3fb8aa3b, v7
	v_cndmask_b32_e32 v1, v9, v1, vcc
	v_cmp_lt_f32_e32 vcc, 0, v0
	v_exp_f32_e32 v14, v14
	v_exp_f32_e32 v15, v15
	v_pk_add_f32 v[10:11], v[10:11], -1.0 op_sel_hi:[1,0]
	v_cndmask_b32_e32 v0, v8, v0, vcc
	v_cmp_lt_f32_e32 vcc, 0, v3
	v_pk_add_f32 v[12:13], v[12:13], -1.0 op_sel_hi:[1,0]
	v_pk_add_f32 v[14:15], v[14:15], -1.0 op_sel_hi:[1,0]
	v_cndmask_b32_e32 v3, v11, v3, vcc
	v_cmp_lt_f32_e32 vcc, 0, v2
	v_cvt_pk_f16_f32 v0, v0, v1
	s_nop 0
	v_cndmask_b32_e32 v2, v10, v2, vcc
	v_cmp_lt_f32_e32 vcc, 0, v5
	v_cvt_pk_f16_f32 v1, v2, v3
	s_nop 0
	v_cndmask_b32_e32 v5, v13, v5, vcc
	v_cmp_lt_f32_e32 vcc, 0, v4
	s_nop 1
	v_cndmask_b32_e32 v4, v12, v4, vcc
	v_cmp_lt_f32_e32 vcc, 0, v7
	v_cvt_pk_f16_f32 v2, v4, v5
	s_nop 0
	v_cndmask_b32_e32 v7, v15, v7, vcc
	v_cmp_lt_f32_e32 vcc, 0, v6
	s_nop 1
	v_cndmask_b32_e32 v6, v14, v6, vcc
	v_cvt_pk_f16_f32 v3, v6, v7
	s_mov_b64 vcc, s[0:1]
	global_store_dword v77, v78, s[38:39]
	ds_write_b128 v16, v[0:3]
	s_cbranch_vccz .LBB3_14
	v_lshlrev_b32_e32 v16, 4, v42
	v_mov_b32_e32 v17, 0
	v_mul_u32_u24_e32 v2, 0x88, v44
	v_lshl_add_u64 v[0:1], s[6:7], 0, v[16:17]
	v_lshlrev_b32_e32 v2, 1, v2
	v_mov_b32_e32 v3, v17
	v_lshl_add_u64 v[18:19], v[0:1], 0, v[2:3]
	v_add_co_u32_e32 v40, vcc, 0x1000, v18
	s_nop 1
	v_addc_co_u32_e32 v41, vcc, 0, v19, vcc
	global_load_dwordx4 v[36:39], v[18:19], off
	global_load_dwordx4 v[28:31], v[18:19], off offset:64
	global_load_dwordx4 v[32:35], v[40:41], off offset:256
	global_load_dwordx4 v[20:23], v[40:41], off offset:320
	global_load_dwordx4 v[12:15], v[18:19], off offset:128
	global_load_dwordx4 v[8:11], v[18:19], off offset:192
	global_load_dwordx4 v[4:7], v[40:41], off offset:384
	global_load_dwordx4 v[0:3], v[40:41], off offset:448
	global_load_dwordx4 v[24:27], v16, s[22:23]
	s_nop 0
	global_load_dwordx4 v[16:19], v16, s[22:23] offset:64
	s_branch .LBB3_15

	.amdhsa_kernel _Z6k_agg1PKiS0_PK6__halfPKfS5_S5_S3_S5_S5_PS1_PfS7_S5_S0_S0_
		.amdhsa_group_segment_fixed_size 5376
		.amdhsa_private_segment_fixed_size 0
		.amdhsa_kernarg_size 120
		.amdhsa_user_sgpr_count 2
		.amdhsa_user_sgpr_dispatch_ptr 0
		.amdhsa_user_sgpr_queue_ptr 0
		.amdhsa_user_sgpr_kernarg_segment_ptr 1
		.amdhsa_user_sgpr_dispatch_id 0
		.amdhsa_user_sgpr_kernarg_preload_length 0
		.amdhsa_user_sgpr_kernarg_preload_offset 0
		.amdhsa_user_sgpr_private_segment_size 0
		.amdhsa_uses_dynamic_stack 0
		.amdhsa_enable_private_segment 0
		.amdhsa_system_sgpr_workgroup_id_x 1
		.amdhsa_system_sgpr_workgroup_id_y 0
		.amdhsa_system_sgpr_workgroup_id_z 0
		.amdhsa_system_sgpr_workgroup_info 0
		.amdhsa_system_vgpr_workitem_id 0
		.amdhsa_next_free_vgpr 79
		.amdhsa_next_free_sgpr 40
		.amdhsa_accum_offset 80
		.amdhsa_reserve_vcc 1
		.amdhsa_float_round_mode_32 0
		.amdhsa_float_round_mode_16_64 0
		.amdhsa_float_denorm_mode_32 3
		.amdhsa_float_denorm_mode_16_64 3
		.amdhsa_dx10_clamp 1
		.amdhsa_ieee_mode 1
		.amdhsa_fp16_overflow 0
		.amdhsa_tg_split 0
		.amdhsa_exception_fp_ieee_invalid_op 0
		.amdhsa_exception_fp_denorm_src 0
		.amdhsa_exception_fp_ieee_div_zero 0
		.amdhsa_exception_fp_ieee_overflow 0
		.amdhsa_exception_fp_ieee_underflow 0
		.amdhsa_exception_fp_ieee_inexact 0
		.amdhsa_exception_int_div_zero 0
	.end_amdhsa_kernel

_Z6k_agg2PKiS0_PK6__halfPKfS5_S5_PfS5_S0_S0_:
	s_and_b32 s3, s2, 7
	s_mul_i32 s8, s3, 0x30d
	s_min_u32 s3, s3, 2
	s_lshr_b32 s2, s2, 3
	s_add_i32 s2, s3, s2
	s_load_dwordx4 s[4:7], s[0:1], 0x38
	v_lshrrev_b32_e32 v1, 6, v0
	s_add_i32 s2, s2, s8
	s_lshl_b32 s12, s2, 4
	v_lshlrev_b32_e32 v2, 2, v1
	v_bfe_u32 v3, v0, 4, 2
	v_or3_b32 v2, s12, v2, v3
	v_ashrrev_i32_e32 v3, 31, v2
	v_lshlrev_b64 v[10:11], 2, v[2:3]
	s_load_dwordx2 s[2:3], s[0:1], 0x48
	s_waitcnt lgkmcnt(0)
	v_lshl_add_u64 v[2:3], s[6:7], 0, v[10:11]
	global_load_dword v17, v[2:3], off
	s_sub_u32 s22, s6, 13200128
	s_subb_u32 s23, s7, 0
	v_and_b32_e32 v60, 15, v0
	v_lshlrev_b32_e32 v61, 4, v10
	v_lshl_add_u32 v60, v60, 2, v61
	global_load_dword v60, v60, s[22:23]
	s_load_dwordx4 s[8:11], s[0:1], 0x20
	s_load_dwordx2 s[16:17], s[0:1], 0x8
	v_and_b32_e32 v29, 3, v0
	v_mov_b32_e32 v15, 0
	v_bfe_u32 v16, v0, 2, 2
	v_lshlrev_b32_e32 v14, 5, v29
	global_load_dwordx4 v[2:5], v14, s[4:5] offset:16
	global_load_dwordx4 v[6:9], v14, s[4:5]
	s_waitcnt lgkmcnt(0)
	v_lshl_add_u64 v[12:13], s[10:11], 0, v[14:15]
	v_lshlrev_b32_e32 v14, 3, v16
	v_lshl_add_u64 v[22:23], v[12:13], 0, v[14:15]
	v_lshl_add_u64 v[10:11], s[2:3], 0, v[10:11]
	global_load_dword v19, v[10:11], off
	v_mov_b32_e32 v41, 0
	s_waitcnt vmcnt(3)
	v_add_u32_sdwa v12, sext(v17), s12 dst_sel:DWORD dst_unused:UNUSED_PAD src0_sel:BYTE_3 src1_sel:DWORD
	v_ashrrev_i32_e32 v13, 31, v12
	v_lshl_add_u64 v[24:25], v[12:13], 2, s[8:9]
	global_load_dword v21, v[24:25], off
	global_load_dwordx2 v[10:11], v[22:23], off
	v_and_b32_e32 v23, 15, v0
	v_and_b32_e32 v24, 0xffffff, v17
	v_add_u32_e32 v14, v24, v23
	s_waitcnt vmcnt(2)
	v_cmp_lt_i32_e32 vcc, v14, v19
	s_nop 1
	v_cndmask_b32_e32 v41, 0, v60, vcc
	v_lshlrev_b32_e32 v17, 3, v29
	v_lshlrev_b32_e32 v14, 1, v16
	v_cmp_gt_i32_e32 vcc, v19, v24
	v_mov_b32_e32 v40, 0xff800000
	v_mov_b32_e32 v18, 0
	v_mov_b32_e32 v20, 0
	v_mov_b32_e32 v22, 0
	v_mov_b32_e32 v25, 0
	v_mov_b32_e32 v26, 0
	v_mov_b32_e32 v27, 0
	v_mov_b32_e32 v28, 0
	v_mov_b32_e32 v38, 0
	s_and_saveexec_b64 s[18:19], vcc
	s_cbranch_execz .LBB4_8
	s_load_dwordx2 s[12:13], s[0:1], 0x10
	v_and_b32_e32 v15, 63, v0
	v_lshlrev_b32_e32 v1, 8, v1
	v_and_or_b32 v0, v0, 48, v16
	s_mov_b32 s15, 0x20000
	s_mov_b32 s14, 0x61a800
	s_waitcnt lgkmcnt(0)
	s_and_b32 s13, s13, 0xffff
	v_lshlrev_b32_e32 v29, 4, v29
	v_lshl_or_b32 v30, v15, 2, v1
	v_lshl_or_b32 v31, v0, 2, v1
	v_or_b32_e32 v32, 4, v16
	v_or_b32_e32 v33, 8, v16
	v_or_b32_e32 v34, 12, v16
	v_cvt_pk_f16_f32 v6, v6, v7
	v_cvt_pk_f16_f32 v7, v8, v9
	v_cvt_pk_f16_f32 v8, v2, v3
	v_cvt_pk_f16_f32 v9, v4, v5
	v_sub_u32_e32 v35, v19, v24
	v_mov_b32_e32 v5, 0
	v_mov_b32_e32 v39, 0xff800000
	s_mov_b64 s[20:21], 0
	v_bfrev_b32_e32 v36, 1
	v_mov_b32_e32 v37, 0xff800000
	v_mov_b32_e32 v38, 0
	v_mov_b32_e32 v28, 0
	v_mov_b32_e32 v27, 0
	v_mov_b32_e32 v26, 0
	v_mov_b32_e32 v25, 0
	v_mov_b32_e32 v22, 0
	v_mov_b32_e32 v20, 0
	v_mov_b32_e32 v18, 0
	v_mov_b32_e32 v15, 0
	s_branch .LBB4_5

	.amdhsa_kernel _Z6k_agg2PKiS0_PK6__halfPKfS5_S5_PfS5_S0_S0_
		.amdhsa_group_segment_fixed_size 1024
		.amdhsa_private_segment_fixed_size 0
		.amdhsa_kernarg_size 80
		.amdhsa_user_sgpr_count 2
		.amdhsa_user_sgpr_dispatch_ptr 0
		.amdhsa_user_sgpr_queue_ptr 0
		.amdhsa_user_sgpr_kernarg_segment_ptr 1
		.amdhsa_user_sgpr_dispatch_id 0
		.amdhsa_user_sgpr_kernarg_preload_length 0
		.amdhsa_user_sgpr_kernarg_preload_offset 0
		.amdhsa_user_sgpr_private_segment_size 0
		.amdhsa_uses_dynamic_stack 0
		.amdhsa_enable_private_segment 0
		.amdhsa_system_sgpr_workgroup_id_x 1
		.amdhsa_system_sgpr_workgroup_id_y 0
		.amdhsa_system_sgpr_workgroup_id_z 0
		.amdhsa_system_sgpr_workgroup_info 0
		.amdhsa_system_vgpr_workitem_id 0
		.amdhsa_next_free_vgpr 62
		.amdhsa_next_free_sgpr 24
		.amdhsa_accum_offset 64
		.amdhsa_reserve_vcc 1
		.amdhsa_float_round_mode_32 0
		.amdhsa_float_round_mode_16_64 0
		.amdhsa_float_denorm_mode_32 3
		.amdhsa_float_denorm_mode_16_64 3
		.amdhsa_dx10_clamp 1
		.amdhsa_ieee_mode 1
		.amdhsa_fp16_overflow 0
		.amdhsa_tg_split 0
		.amdhsa_exception_fp_ieee_invalid_op 0
		.amdhsa_exception_fp_denorm_src 0
		.amdhsa_exception_fp_ieee_div_zero 0
		.amdhsa_exception_fp_ieee_overflow 0
		.amdhsa_exception_fp_ieee_underflow 0
		.amdhsa_exception_fp_ieee_inexact 0
		.amdhsa_exception_int_div_zero 0
	.end_amdhsa_kernel

amdhsa.kernels:
  - .agpr_count:     0
    .args:
      - .actual_access:  read_only
        .address_space:  global
        .offset:         0
        .size:           8
        .value_kind:     global_buffer
      - .actual_access:  read_only
        .address_space:  global
        .offset:         8
        .size:           8
        .value_kind:     global_buffer
      - .actual_access:  write_only
        .address_space:  global
        .offset:         16
        .size:           8
        .value_kind:     global_buffer
      - .actual_access:  write_only
        .address_space:  global
        .offset:         24
        .size:           8
        .value_kind:     global_buffer
      - .actual_access:  write_only
        .address_space:  global
        .offset:         32
        .size:           8
        .value_kind:     global_buffer
    .group_segment_fixed_size: 0
    .kernarg_segment_align: 8
    .kernarg_segment_size: 40
    .language:       OpenCL C
    .language_version:
      - 2
      - 0
    .max_flat_workgroup_size: 256
    .name:           _Z6k_prepPKfS0_P6__halfS2_Pi
    .private_segment_fixed_size: 0
    .sgpr_count:     18
    .sgpr_spill_count: 0
    .symbol:         _Z6k_prepPKfS0_P6__halfS2_Pi.kd
    .uniform_work_group_size: 1
    .uses_dynamic_stack: false
    .vgpr_count:     6
    .vgpr_spill_count: 0
    .wavefront_size: 64
  - .agpr_count:     0
    .args:
      - .actual_access:  read_only
        .address_space:  global
        .offset:         0
        .size:           8
        .value_kind:     global_buffer
      - .actual_access:  read_only
        .address_space:  global
        .offset:         8
        .size:           8
        .value_kind:     global_buffer
      - .address_space:  global
        .offset:         16
        .size:           8
        .value_kind:     global_buffer
      - .actual_access:  write_only
        .address_space:  global
        .offset:         24
        .size:           8
        .value_kind:     global_buffer
      - .actual_access:  write_only
        .address_space:  global
        .offset:         32
        .size:           8
        .value_kind:     global_buffer
      - .actual_access:  read_only
        .address_space:  global
        .offset:         40
        .size:           8
        .value_kind:     global_buffer
      - .actual_access:  read_only
        .address_space:  global
        .offset:         48
        .size:           8
        .value_kind:     global_buffer
      - .actual_access:  read_only
        .address_space:  global
        .offset:         56
        .size:           8
        .value_kind:     global_buffer
      - .actual_access:  read_only
        .address_space:  global
        .offset:         64
        .size:           8
        .value_kind:     global_buffer
      - .actual_access:  write_only
        .address_space:  global
        .offset:         72
        .size:           8
        .value_kind:     global_buffer
      - .actual_access:  read_only
        .address_space:  global
        .offset:         80
        .size:           8
        .value_kind:     global_buffer
      - .actual_access:  write_only
        .address_space:  global
        .offset:         88
        .size:           8
        .value_kind:     global_buffer
    .group_segment_fixed_size: 53248
    .kernarg_segment_align: 8
    .kernarg_segment_size: 96
    .language:       OpenCL C
    .language_version:
      - 2
      - 0
    .max_flat_workgroup_size: 256
    .name:           _Z15k_scatter_gemm1PKiS0_PiPjPyPKfPK6__halfS5_S5_PS6_PfSA_
    .private_segment_fixed_size: 0
    .sgpr_count:     32
    .sgpr_spill_count: 0
    .symbol:         _Z15k_scatter_gemm1PKiS0_PiPjPyPKfPK6__halfS5_S5_PS6_PfSA_.kd
    .uniform_work_group_size: 1
    .uses_dynamic_stack: false
    .vgpr_count:     146
    .vgpr_spill_count: 0
    .wavefront_size: 64
  - .agpr_count:     0
    .args:
      - .actual_access:  read_only
        .address_space:  global
        .offset:         0
        .size:           8
        .value_kind:     global_buffer
      - .actual_access:  read_only
        .address_space:  global
        .offset:         8
        .size:           8
        .value_kind:     global_buffer
      - .actual_access:  read_only
        .address_space:  global
        .offset:         16
        .size:           8
        .value_kind:     global_buffer
      - .actual_access:  write_only
        .address_space:  global
        .offset:         24
        .size:           8
        .value_kind:     global_buffer
      - .actual_access:  write_only
        .address_space:  global
        .offset:         32
        .size:           8
        .value_kind:     global_buffer
      - .actual_access:  write_only
        .address_space:  global
        .offset:         40
        .size:           8
        .value_kind:     global_buffer
      - .actual_access:  write_only
        .address_space:  global
        .offset:         48
        .size:           8
        .value_kind:     global_buffer
      - .actual_access:  read_only
        .address_space:  global
        .offset:         56
        .size:           8
        .value_kind:     global_buffer
      - .actual_access:  read_only
        .address_space:  global
        .offset:         64
        .size:           8
        .value_kind:     global_buffer
      - .actual_access:  read_only
        .address_space:  global
        .offset:         72
        .size:           8
        .value_kind:     global_buffer
      - .actual_access:  read_only
        .address_space:  global
        .offset:         80
        .size:           8
        .value_kind:     global_buffer
      - .actual_access:  write_only
        .address_space:  global
        .offset:         88
        .size:           8
        .value_kind:     global_buffer
      - .actual_access:  read_only
        .address_space:  global
        .offset:         96
        .size:           8
        .value_kind:     global_buffer
      - .actual_access:  write_only
        .address_space:  global
        .offset:         104
        .size:           8
        .value_kind:     global_buffer
    .group_segment_fixed_size: 53248
    .kernarg_segment_align: 8
    .kernarg_segment_size: 112
    .language:       OpenCL C
    .language_version:
      - 2
      - 0
    .max_flat_workgroup_size: 256
    .name:           _Z12k_fine_gemm1PKjPKyPKiPiS5_S5_S5_PKfPK6__halfS7_S7_PS8_PfSC_
    .private_segment_fixed_size: 0
    .sgpr_count:     102
    .sgpr_spill_count: 0
    .symbol:         _Z12k_fine_gemm1PKjPKyPKiPiS5_S5_S5_PKfPK6__halfS7_S7_PS8_PfSC_.kd
    .uniform_work_group_size: 1
    .uses_dynamic_stack: false
    .vgpr_count:     144
    .vgpr_spill_count: 0
    .wavefront_size: 64
  - .agpr_count:     0
    .args:
      - .actual_access:  read_only
        .address_space:  global
        .offset:         0
        .size:           8
        .value_kind:     global_buffer
      - .actual_access:  read_only
        .address_space:  global
        .offset:         8
        .size:           8
        .value_kind:     global_buffer
      - .actual_access:  read_only
        .address_space:  global
        .offset:         16
        .size:           8
        .value_kind:     global_buffer
      - .actual_access:  read_only
        .address_space:  global
        .offset:         24
        .size:           8
        .value_kind:     global_buffer
      - .actual_access:  read_only
        .address_space:  global
        .offset:         32
        .size:           8
        .value_kind:     global_buffer
      - .actual_access:  read_only
        .address_space:  global
        .offset:         40
        .size:           8
        .value_kind:     global_buffer
      - .actual_access:  read_only
        .address_space:  global
        .offset:         48
        .size:           8
        .value_kind:     global_buffer
      - .actual_access:  read_only
        .address_space:  global
        .offset:         56
        .size:           8
        .value_kind:     global_buffer
      - .actual_access:  read_only
        .address_space:  global
        .offset:         64
        .size:           8
        .value_kind:     global_buffer
      - .actual_access:  write_only
        .address_space:  global
        .offset:         72
        .size:           8
        .value_kind:     global_buffer
      - .actual_access:  read_only
        .address_space:  global
        .offset:         80
        .size:           8
        .value_kind:     global_buffer
      - .actual_access:  write_only
        .address_space:  global
        .offset:         88
        .size:           8
        .value_kind:     global_buffer
      - .actual_access:  read_only
        .address_space:  global
        .offset:         96
        .size:           8
        .value_kind:     global_buffer
      - .actual_access:  read_only
        .address_space:  global
        .offset:         104
        .size:           8
        .value_kind:     global_buffer
      - .actual_access:  read_only
        .address_space:  global
        .offset:         112
        .size:           8
        .value_kind:     global_buffer
    .group_segment_fixed_size: 5376
    .kernarg_segment_align: 8
    .kernarg_segment_size: 120
    .language:       OpenCL C
    .language_version:
      - 2
      - 0
    .max_flat_workgroup_size: 256
    .name:           _Z6k_agg1PKiS0_PK6__halfPKfS5_S5_S3_S5_S5_PS1_PfS7_S5_S0_S0_
    .private_segment_fixed_size: 0
    .sgpr_count:     46
    .sgpr_spill_count: 0
    .symbol:         _Z6k_agg1PKiS0_PK6__halfPKfS5_S5_S3_S5_S5_PS1_PfS7_S5_S0_S0_.kd
    .uniform_work_group_size: 1
    .uses_dynamic_stack: false
    .vgpr_count:     79
    .vgpr_spill_count: 0
    .wavefront_size: 64
  - .agpr_count:     0
    .args:
      - .actual_access:  read_only
        .address_space:  global
        .offset:         0
        .size:           8
        .value_kind:     global_buffer
      - .actual_access:  read_only
        .address_space:  global
        .offset:         8
        .size:           8
        .value_kind:     global_buffer
      - .actual_access:  read_only
        .address_space:  global
        .offset:         16
        .size:           8
        .value_kind:     global_buffer
      - .actual_access:  read_only
        .address_space:  global
        .offset:         24
        .size:           8
        .value_kind:     global_buffer
      - .actual_access:  read_only
        .address_space:  global
        .offset:         32
        .size:           8
        .value_kind:     global_buffer
      - .actual_access:  read_only
        .address_space:  global
        .offset:         40
        .size:           8
        .value_kind:     global_buffer
      - .actual_access:  write_only
        .address_space:  global
        .offset:         48
        .size:           8
        .value_kind:     global_buffer
      - .actual_access:  read_only
        .address_space:  global
        .offset:         56
        .size:           8
        .value_kind:     global_buffer
      - .actual_access:  read_only
        .address_space:  global
        .offset:         64
        .size:           8
        .value_kind:     global_buffer
      - .actual_access:  read_only
        .address_space:  global
        .offset:         72
        .size:           8
        .value_kind:     global_buffer
    .group_segment_fixed_size: 1024
    .kernarg_segment_align: 8
    .kernarg_segment_size: 80
    .language:       OpenCL C
    .language_version:
      - 2
      - 0
    .max_flat_workgroup_size: 256
    .name:           _Z6k_agg2PKiS0_PK6__halfPKfS5_S5_PfS5_S0_S0_
    .private_segment_fixed_size: 0
    .sgpr_count:     30
    .sgpr_spill_count: 0
    .symbol:         _Z6k_agg2PKiS0_PK6__halfPKfS5_S5_PfS5_S0_S0_.kd
    .uniform_work_group_size: 1
    .uses_dynamic_stack: false
    .vgpr_count:     62
    .vgpr_spill_count: 0
    .wavefront_size: 64
